# P2: conditional bf16 row loads issued without per-load vmcnt(0) drains (widened after the single phase drain)
# speedup vs baseline: 1.0130x; 1.0050x over previous
; #define GAS __attribute__((address_space(1)))
; __global__ void __launch_bounds__(NTHR, 2) mk_fwd(Args args) {
;     ...
;         for (int q = 0; q < 5; ++q) { const int i = lane + 64 * q; prevl[q] = (i < 288 && t0 > 0) ? ld1bf(PROJ + (size_t)(m0 - 1) * IN_PAD + 3072 + i) : 0.f; }
; #pragma unroll
;         for (int i8 = 0; i8 < 8; ++i8) {
; #pragma unroll
;             for (int q = 0; q < 5; ++q) { const int i = lane + 64 * q; rl[i8][q] = i < 288 ? *(const GAS bf16*)(PROJ + (size_t)(m0 + i8) * IN_PAD + 3072 + i) : (bf16)0; }
; #pragma unroll
;             for (int q = 0; q < 4; ++q) rc[i8][q] = *(const GAS v2u*)(PROJ + (size_t)(m0 + i8) * IN_PAD + SHIFT_W + 4 * lane + 256 * q);
;         }
.LBB0_188:
	s_or_b64 exec, exec, s[4:5]
	s_bfe_i32 s2, s30, 0x1001c
	s_lshl_b32 s84, s30, 3
	s_lshr_b32 s2, s2, 20
	s_add_i32 s2, s84, s2
	s_and_b32 s2, s2, 0xfffff000
	s_sub_i32 s36, s84, s2
	s_cmp_gt_i32 s36, 0
	s_cselect_b64 s[6:7], -1, 0
	s_add_i32 s2, s84, -1
	s_mul_hi_i32 s3, s2, 0x2400
	s_mulk_i32 s2, 0x2400
	s_add_u32 s86, s10, s2
	s_addc_u32 s87, s11, s3
	s_add_u32 s4, s86, 0x1800
	s_addc_u32 s5, s87, 0
	s_cmp_lt_i32 s36, 1
	s_cbranch_scc1 .LBB0_190
	v_lshlrev_b32_e32 v2, 1, v194
	global_load_ushort v39, v2, s[4:5]
.LBB0_190:
	v_or_b32_e32 v2, 64, v194
	v_cndmask_b32_e64 v3, 0, 1, s[6:7]
	v_mov_b32_e32 v92, 0
	v_cmp_ne_u32_e64 s[2:3], 1, v3
	s_andn2_b64 vcc, exec, s[6:7]
	v_lshlrev_b32_e32 v6, 1, v2
	v_mov_b32_e32 v75, 0
	s_cbranch_vccnz .LBB0_192
	global_load_ushort v75, v6, s[4:5]
.LBB0_192:
	v_or_b32_e32 v2, 0x80, v194
	s_and_b64 vcc, exec, s[2:3]
	v_lshlrev_b32_e32 v7, 1, v2
	s_cbranch_vccnz .LBB0_194
	global_load_ushort v92, v7, s[4:5]
.LBB0_194:
	v_or_b32_e32 v2, 0xc0, v194
	v_mov_b32_e32 v184, 0
	s_and_b64 vcc, exec, s[2:3]
	v_lshlrev_b32_e32 v8, 1, v2
	v_mov_b32_e32 v93, 0
	s_cbranch_vccnz .LBB0_196
	global_load_ushort v93, v8, s[4:5]
.LBB0_196:
	v_or_b32_e32 v9, 0x100, v194
	s_movk_i32 s2, 0x120
	v_cmp_gt_u32_e64 s[2:3], s2, v9
	s_and_b64 s[8:9], s[2:3], s[6:7]
	s_and_saveexec_b64 s[6:7], s[8:9]
	s_cbranch_execz .LBB0_198
	v_lshlrev_b32_e32 v2, 1, v9
	global_load_ushort v184, v2, s[4:5]
.LBB0_198:
	s_or_b64 exec, exec, s[6:7]
	s_mul_i32 s4, s84, 0x2400
	s_mul_hi_i32 s5, s84, 0x2400
	s_add_u32 s4, s10, s4
	s_addc_u32 s5, s11, s5
	s_add_u32 s6, s4, 0x1800
	s_addc_u32 s7, s5, 0
	v_lshlrev_b32_e32 v4, 1, v194
	global_load_ushort v5, v4, s[6:7]
	global_load_ushort v95, v6, s[6:7]
	global_load_ushort v108, v7, s[6:7]
	global_load_ushort v94, v8, s[6:7]
	v_mov_b32_e32 v91, 0
	v_mov_b32_e32 v74, 0
	s_and_saveexec_b64 s[8:9], s[2:3]
	s_cbranch_execz .LBB0_200
	v_lshlrev_b32_e32 v2, 1, v9
	global_load_ushort v74, v2, s[6:7]
.LBB0_200:
	s_or_b64 exec, exec, s[8:9]
	s_or_b32 s82, s84, 1
	s_mul_i32 s6, s82, 0x2400
	v_lshlrev_b32_e32 v90, 3, v194
	s_mul_hi_i32 s7, s82, 0x2400
	s_add_u32 s6, s10, s6
	v_lshl_add_u64 v[2:3], s[4:5], 0, v[90:91]
	s_mov_b64 s[4:5], 0x1a40
	s_addc_u32 s7, s11, s7
	v_lshl_add_u64 v[10:11], v[2:3], 0, s[4:5]
	v_add_co_u32_e32 v2, vcc, 0x1000, v2
	s_add_u32 s8, s6, 0x1800
	s_nop 0
	v_addc_co_u32_e32 v3, vcc, 0, v3, vcc
	s_addc_u32 s9, s7, 0
	global_load_dwordx2 v[106:107], v[2:3], off offset:2624
	global_load_dwordx2 v[104:105], v[10:11], off offset:512
	global_load_dwordx2 v[102:103], v[10:11], off offset:1024
	global_load_dwordx2 v[100:101], v[10:11], off offset:1536
	global_load_ushort v214, v4, s[8:9]
	global_load_ushort v212, v6, s[8:9]
	global_load_ushort v213, v7, s[8:9]
	global_load_ushort v90, v8, s[8:9]
	s_and_saveexec_b64 s[14:15], s[2:3]
	s_cbranch_execz .LBB0_202
	v_lshlrev_b32_e32 v2, 1, v9
	global_load_ushort v91, v2, s[8:9]
.LBB0_202:
	s_or_b64 exec, exec, s[14:15]
	v_lshlrev_b32_e32 v2, 1, v38
	v_mov_b32_e32 v3, 0
	v_lshl_add_u64 v[10:11], s[6:7], 0, v[2:3]
	s_or_b32 s80, s84, 2
	v_lshl_add_u64 v[12:13], v[10:11], 0, s[4:5]
	s_mul_i32 s4, s80, 0x2400
	s_mul_hi_i32 s5, s80, 0x2400
	s_add_u32 s4, s10, s4
	s_addc_u32 s5, s11, s5
	v_add_co_u32_e32 v10, vcc, 0x1000, v10
	s_add_u32 s6, s4, 0x1800
	s_nop 0
	v_addc_co_u32_e32 v11, vcc, 0, v11, vcc
	s_addc_u32 s7, s5, 0
	global_load_dwordx2 v[88:89], v[10:11], off offset:2624
	global_load_dwordx2 v[86:87], v[12:13], off offset:512
	global_load_dwordx2 v[84:85], v[12:13], off offset:1024
	global_load_dwordx2 v[82:83], v[12:13], off offset:1536
	global_load_ushort v211, v4, s[6:7]
	global_load_ushort v209, v6, s[6:7]
	global_load_ushort v210, v7, s[6:7]
	global_load_ushort v208, v8, s[6:7]
	v_mov_b32_e32 v207, v3
	s_and_saveexec_b64 s[8:9], s[2:3]
	s_cbranch_execz .LBB0_204
	v_lshlrev_b32_e32 v10, 1, v9
	global_load_ushort v207, v10, s[6:7]

; #define GAS __attribute__((address_space(1)))
; __global__ void __launch_bounds__(NTHR, 2) mk_fwd(Args args) {
;     ...
;         for (int i8 = 0; i8 < 8; ++i8) {
; #pragma unroll
;             for (int q = 0; q < 5; ++q) { const int i = lane + 64 * q; rl[i8][q] = i < 288 ? *(const GAS bf16*)(PROJ + (size_t)(m0 + i8) * IN_PAD + 3072 + i) : (bf16)0; }
; #pragma unroll
;             for (int q = 0; q < 4; ++q) rc[i8][q] = *(const GAS v2u*)(PROJ + (size_t)(m0 + i8) * IN_PAD + SHIFT_W + 4 * lane + 256 * q);
;         }
.LBB0_206:
	s_or_b64 exec, exec, s[14:15]
	v_mov_b32_e32 v31, 0
	v_mov_b32_e32 v30, v2
	v_lshl_add_u64 v[10:11], s[6:7], 0, v[30:31]
	s_or_b32 s66, s84, 4
	v_lshl_add_u64 v[12:13], v[10:11], 0, s[4:5]
	s_mul_i32 s4, s66, 0x2400
	s_mul_hi_i32 s5, s66, 0x2400
	s_add_u32 s4, s10, s4
	s_addc_u32 s5, s11, s5
	v_add_co_u32_e32 v10, vcc, 0x1000, v10
	s_add_u32 s6, s4, 0x1800
	s_nop 0
	v_addc_co_u32_e32 v11, vcc, 0, v11, vcc
	s_addc_u32 s7, s5, 0
	global_load_dwordx2 v[60:61], v[10:11], off offset:2624
	global_load_dwordx2 v[54:55], v[12:13], off offset:512
	global_load_dwordx2 v[52:53], v[12:13], off offset:1024
	global_load_dwordx2 v[50:51], v[12:13], off offset:1536
	global_load_ushort v202, v4, s[6:7]
	global_load_ushort v200, v6, s[6:7]
	global_load_ushort v201, v7, s[6:7]
	global_load_ushort v199, v8, s[6:7]
	v_mov_b32_e32 v198, v31
	s_and_saveexec_b64 s[8:9], s[2:3]
	s_cbranch_execz .LBB0_208
	v_lshlrev_b32_e32 v10, 1, v9
	global_load_ushort v198, v10, s[6:7]
.LBB0_208:
	s_or_b64 exec, exec, s[8:9]
	s_or_b32 s62, s84, 5
	s_mul_i32 s6, s62, 0x2400
	s_mul_hi_i32 s7, s62, 0x2400
	s_add_u32 s6, s10, s6
	v_lshl_add_u64 v[10:11], s[4:5], 0, v[30:31]
	s_mov_b64 s[4:5], 0x1a40
	s_addc_u32 s7, s11, s7
	v_lshl_add_u64 v[12:13], v[10:11], 0, s[4:5]
	v_add_co_u32_e32 v10, vcc, 0x1000, v10
	s_add_u32 s8, s6, 0x1800
	s_nop 0
	v_addc_co_u32_e32 v11, vcc, 0, v11, vcc
	s_addc_u32 s9, s7, 0
	global_load_dwordx2 v[44:45], v[10:11], off offset:2624
	global_load_dwordx2 v[42:43], v[12:13], off offset:512
	global_load_dwordx2 v[36:37], v[12:13], off offset:1024
	global_load_dwordx2 v[34:35], v[12:13], off offset:1536
	global_load_ushort v197, v4, s[8:9]
	global_load_ushort v193, v6, s[8:9]
	global_load_ushort v196, v7, s[8:9]
	global_load_ushort v30, v8, s[8:9]
	s_and_saveexec_b64 s[14:15], s[2:3]
	s_cbranch_execz .LBB0_210
	v_lshlrev_b32_e32 v10, 1, v9
	global_load_ushort v31, v10, s[8:9]
.LBB0_210:
	s_or_b64 exec, exec, s[14:15]
	v_mov_b32_e32 v13, 0
	v_mov_b32_e32 v12, v2
	v_lshl_add_u64 v[10:11], s[6:7], 0, v[12:13]
	s_or_b32 s16, s84, 6
	v_lshl_add_u64 v[14:15], v[10:11], 0, s[4:5]
	s_mul_i32 s4, s16, 0x2400
	s_mul_hi_i32 s5, s16, 0x2400
	s_add_u32 s4, s10, s4
	s_addc_u32 s5, s11, s5
	v_add_co_u32_e32 v10, vcc, 0x1000, v10
	s_add_u32 s6, s4, 0x1800
	s_nop 0
	v_addc_co_u32_e32 v11, vcc, 0, v11, vcc
	s_addc_u32 s7, s5, 0
	global_load_dwordx2 v[32:33], v[10:11], off offset:2624
	global_load_dwordx2 v[28:29], v[14:15], off offset:512
	global_load_dwordx2 v[26:27], v[14:15], off offset:1024
	global_load_dwordx2 v[24:25], v[14:15], off offset:1536
	global_load_ushort v192, v4, s[6:7]
	global_load_ushort v190, v6, s[6:7]
	global_load_ushort v191, v7, s[6:7]
	global_load_ushort v189, v8, s[6:7]
	v_mov_b32_e32 v188, v13
	s_and_saveexec_b64 s[8:9], s[2:3]
	s_cbranch_execz .LBB0_212
	v_lshlrev_b32_e32 v10, 1, v9
	global_load_ushort v188, v10, s[6:7]
.LBB0_212:
	s_or_b64 exec, exec, s[8:9]
	s_or_b32 s14, s84, 7
	s_mul_i32 s6, s14, 0x2400
	s_mul_hi_i32 s7, s14, 0x2400
	s_add_u32 s6, s10, s6
	v_lshl_add_u64 v[10:11], s[4:5], 0, v[12:13]
	s_mov_b64 s[4:5], 0x1a40
	s_addc_u32 s7, s11, s7
	v_lshl_add_u64 v[14:15], v[10:11], 0, s[4:5]
	v_add_co_u32_e32 v10, vcc, 0x1000, v10
	s_add_u32 s8, s6, 0x1800
	s_nop 0
	v_addc_co_u32_e32 v11, vcc, 0, v11, vcc
	s_addc_u32 s9, s7, 0
	global_load_dwordx2 v[22:23], v[10:11], off offset:2624
	global_load_dwordx2 v[20:21], v[14:15], off offset:512
	global_load_dwordx2 v[18:19], v[14:15], off offset:1024
	global_load_dwordx2 v[16:17], v[14:15], off offset:1536
	global_load_ushort v187, v4, s[8:9]
	global_load_ushort v185, v6, s[8:9]
	global_load_ushort v186, v7, s[8:9]
	global_load_ushort v12, v8, s[8:9]
	s_and_saveexec_b64 s[34:35], s[2:3]
	s_cbranch_execz .LBB0_214
	v_lshlrev_b32_e32 v6, 1, v9
	global_load_ushort v13, v6, s[8:9]

; #define GAS __attribute__((address_space(1)))
; __global__ void __launch_bounds__(NTHR, 2) mk_fwd(Args args) {
;     ...
;         for (int q = 0; q < 5; ++q) { const int i = lane + 64 * q; prevl[q] = (i < 288 && t0 > 0) ? ld1bf(PROJ + (size_t)(m0 - 1) * IN_PAD + 3072 + i) : 0.f; }
; #pragma unroll
;         for (int i8 = 0; i8 < 8; ++i8) {
; #pragma unroll
;             for (int q = 0; q < 5; ++q) { const int i = lane + 64 * q; rl[i8][q] = i < 288 ? *(const GAS bf16*)(PROJ + (size_t)(m0 + i8) * IN_PAD + 3072 + i) : (bf16)0; }
;     ...
;                 if (q < 5) { if (i < 288) { const float cur = __builtin_bit_cast(float, (unsigned)rl[i8][q < 5 ? q : 0] << 16); const float s_ = cur + (prevl[q < 5 ? q : 0] - cur) * mu_l[q < 5 ? q : 0]; prevl[q < 5 ? q : 0] = cur;
;                     v = i < 64 ? tanhf(s_) : (i < 128 ? s_ : 1.0f / (1.0f + __expf(-s_))); } }
.LBB0_266:
	s_waitcnt vmcnt(0)
	v_lshlrev_b32_e32 v39, 16, v39
	v_lshlrev_b32_e32 v75, 16, v75
	v_lshlrev_b32_e32 v92, 16, v92
	v_lshlrev_b32_e32 v93, 16, v93
	v_lshlrev_b32_e32 v184, 16, v184
	v_lshlrev_b32_e32 v74, 16, v74
	v_lshlrev_b32_e32 v91, 16, v91
	v_lshlrev_b32_e32 v207, 16, v207
	v_lshlrev_b32_e32 v3, 16, v3
	v_lshlrev_b32_e32 v198, 16, v198
	v_lshlrev_b32_e32 v31, 16, v31
	v_lshlrev_b32_e32 v188, 16, v188
	v_lshlrev_b32_e32 v13, 16, v13
	v_lshlrev_b32_e32 v215, 16, v5
	v_sub_f32_e32 v5, v39, v215
	v_fma_f32 v5, v183, v5, v215
	s_mov_b32 s4, 0x3f200000
	v_cmp_nlt_f32_e64 s[4:5], |v5|, s4
	s_and_saveexec_b64 s[6:7], s[4:5]
	s_xor_b64 s[4:5], exec, s[6:7]
	s_cbranch_execz .LBB0_268
	v_add_f32_e64 v38, |v5|, |v5|
	v_mul_f32_e32 v39, 0x3fb8aa3b, v38
	s_mov_b32 s6, 0x3fb8aa3b
	v_rndne_f32_e32 v40, v39
	v_sub_f32_e32 v48, v39, v40
	v_fma_f32 v39, v38, s6, -v39
	v_fmamk_f32 v39, v38, 0x32a5705f, v39
	v_add_f32_e32 v39, v48, v39
	v_exp_f32_e32 v39, v39
	v_cvt_i32_f32_e32 v40, v40
	s_mov_b32 s6, 0xc2ce8ed0
	v_cmp_ngt_f32_e32 vcc, s6, v38
	s_mov_b32 s6, 0x42b17218
	v_ldexp_f32 v39, v39, v40
	v_cndmask_b32_e32 v39, 0, v39, vcc
	v_mov_b32_e32 v40, 0x7f800000
	v_cmp_nlt_f32_e32 vcc, s6, v38
	s_nop 1
	v_cndmask_b32_e32 v38, v40, v39, vcc
	v_add_f32_e32 v38, 1.0, v38
	v_rcp_f32_e32 v38, v38
	s_nop 0
	v_fma_f32 v38, v38, -2.0, 1.0
